# P2 softmax VALU diet: 11-op max trees -> 4 ops (v_max3), NaN-canonicalising max(x,x) removed, tile-1 sum adds moved into the MFMA->VALU wait slot, +0 sum starts removed
# speedup vs baseline: 1.0111x; 1.0111x over previous
.LBB0_749:
	s_add_i32 s29, s18, 3
	s_min_i32 s29, s29, 11
	s_add_i32 s29, s29, s28
	s_waitcnt vmcnt(18)
	v_med3_i32 v54, s29, 0, v184
	v_lshl_or_b32 v2, v54, 11, v160
	v_lshl_add_u64 v[4:5], v[104:105], 0, v[2:3]
	v_lshlrev_b32_e32 v2, 12, v54
	global_load_dwordx4 v[46:49], v[4:5], off
	global_load_dwordx4 v[50:53], v[4:5], off offset:1024
	v_lshl_add_u64 v[4:5], v[106:107], 0, v[2:3]
	global_load_dwordx4 v[54:57], v[4:5], off
	global_load_dwordx4 v[58:61], v[4:5], off offset:1024
	global_load_dwordx4 v[62:65], v[4:5], off offset:2048
	global_load_dwordx4 v[66:69], v[4:5], off offset:3072
	s_add_i32 s29, s15, s18
	s_cmpk_gt_u32 s29, 0xff
	s_cbranch_scc1 .LBB0_755
	s_waitcnt vmcnt(14)
	ds_read2_b32 v[94:95], v108 offset0:8 offset1:9
	ds_read2_b32 v[96:97], v108 offset0:10 offset1:11
	ds_read2_b32 v[116:117], v108 offset0:24 offset1:25
	ds_read2_b32 v[118:119], v108 offset0:26 offset1:27
	s_waitcnt vmcnt(11) lgkmcnt(2)
	v_mfma_f32_16x16x32_fp8_fp8 v[94:97], v[90:91], v[38:39], v[94:97]
	v_mfma_f32_16x16x32_fp8_fp8 v[98:101], v[92:93], v[40:41], v[94:97]
	s_waitcnt vmcnt(10) lgkmcnt(0)
	v_mfma_f32_16x16x32_fp8_fp8 v[94:97], v[86:87], v[38:39], v[116:119]
	v_mfma_f32_16x16x32_fp8_fp8 v[94:97], v[88:89], v[40:41], v[94:97]
	s_nop 4
	v_max3_f32 v2, v98, v99, v100
	s_nop 1
	v_max3_f32 v5, v101, v94, v95
	v_max3_f32 v2, v2, v96, v97
	v_max_f32_e32 v2, v2, v5
	v_mov_b32_e32 v4, v2
	s_nop 1
	v_permlane16_swap_b32_e32 v2, v4
	v_max_f32_e32 v2, v2, v4
	v_mov_b32_e32 v4, v2
	s_nop 1
	v_permlane32_swap_b32_e32 v2, v4
	v_max_f32_e32 v2, v2, v4
	v_cmp_gt_f32_e32 vcc, v2, v112
	s_cbranch_vccz .LBB0_752
	v_max_f32_e32 v2, v2, v2
	v_max_f32_e32 v4, v112, v112
	v_max_f32_e32 v4, v4, v2
	v_sub_f32_e32 v2, v112, v4
	v_exp_f32_e32 v2, v2
	v_mov_b32_e32 v112, v4
	v_mul_f32_e32 v113, v113, v2
	v_pk_mul_f32 v[36:37], v[36:37], v[2:3] op_sel_hi:[1,0]
	v_pk_mul_f32 v[34:35], v[34:35], v[2:3] op_sel_hi:[1,0]
	v_pk_mul_f32 v[32:33], v[32:33], v[2:3] op_sel_hi:[1,0]
	v_pk_mul_f32 v[30:31], v[30:31], v[2:3] op_sel_hi:[1,0]
	v_pk_mul_f32 v[28:29], v[28:29], v[2:3] op_sel_hi:[1,0]
	v_pk_mul_f32 v[26:27], v[26:27], v[2:3] op_sel_hi:[1,0]
	v_pk_mul_f32 v[24:25], v[24:25], v[2:3] op_sel_hi:[1,0]
	v_pk_mul_f32 v[22:23], v[22:23], v[2:3] op_sel_hi:[1,0]
.LBB0_752:
	v_sub_f32_e32 v2, v98, v112
	v_sub_f32_e32 v4, v99, v112
	v_sub_f32_e32 v5, v100, v112
	v_sub_f32_e32 v98, v101, v112
	v_sub_f32_e32 v94, v94, v112
	v_sub_f32_e32 v95, v95, v112
	v_sub_f32_e32 v96, v96, v112
	v_sub_f32_e32 v97, v97, v112
	v_exp_f32_e32 v2, v2
	v_exp_f32_e32 v4, v4
	v_exp_f32_e32 v5, v5
	v_exp_f32_e32 v98, v98
	v_exp_f32_e32 v94, v94
	v_exp_f32_e32 v95, v95
	v_exp_f32_e32 v96, v96
	v_exp_f32_e32 v97, v97
	v_cvt_pk_bf16_f32 v116, v2, v4
	v_cvt_pk_bf16_f32 v117, v5, v98
	v_cvt_pk_bf16_f32 v118, v94, v95
	v_cvt_pk_bf16_f32 v119, v96, v97
	s_waitcnt vmcnt(9)
	s_nop 0
	v_mfma_f32_16x16x32_bf16 v[34:37], v[82:85], v[116:119], v[34:37]
	s_waitcnt vmcnt(8)
	v_mfma_f32_16x16x32_bf16 v[30:33], v[78:81], v[116:119], v[30:33]
	s_waitcnt vmcnt(7)
	v_mfma_f32_16x16x32_bf16 v[26:29], v[74:77], v[116:119], v[26:29]
	s_waitcnt vmcnt(6)
	v_mfma_f32_16x16x32_bf16 v[22:25], v[70:73], v[116:119], v[22:25]
	ds_read2_b32 v[116:117], v108 offset1:1
	ds_read2_b32 v[118:119], v108 offset0:2 offset1:3
	ds_read2_b32 v[120:121], v108 offset0:16 offset1:17
	ds_read2_b32 v[122:123], v108 offset0:18 offset1:19
	s_waitcnt lgkmcnt(2)
	v_mfma_f32_16x16x32_fp8_fp8 v[116:119], v[90:91], v[42:43], v[116:119]
	v_mfma_f32_16x16x32_fp8_fp8 v[90:93], v[92:93], v[44:45], v[116:119]
	s_waitcnt lgkmcnt(0)
	v_mfma_f32_16x16x32_fp8_fp8 v[116:119], v[86:87], v[42:43], v[120:123]
	v_mfma_f32_16x16x32_fp8_fp8 v[86:89], v[88:89], v[44:45], v[116:119]
	v_add_f32_e32 v2, v4, v2
	v_add_f32_e32 v2, v5, v2
	v_add_f32_e32 v2, v98, v2
	v_add_f32_e32 v2, v94, v2
	v_add_f32_e32 v2, v95, v2
	v_add_f32_e32 v2, v96, v2
	v_add_f32_e32 v2, v97, v2
	v_add_f32_e32 v113, v113, v2
	v_max3_f32 v99, v90, v91, v92
	v_max3_f32 v101, v93, v86, v87
	v_max3_f32 v99, v99, v88, v89
	v_max_f32_e32 v99, v99, v101
	v_mov_b32_e32 v100, v99
	s_nop 1
	v_permlane16_swap_b32_e32 v99, v100
	v_max_f32_e32 v99, v99, v100
	v_mov_b32_e32 v100, v99
	s_nop 1
	v_permlane32_swap_b32_e32 v99, v100
	v_max_f32_e32 v99, v99, v100
	v_cmp_gt_f32_e32 vcc, v99, v114
	s_cbranch_vccz .LBB0_754
	v_max_f32_e32 v99, v99, v99
	v_max_f32_e32 v100, v114, v114
	v_max_f32_e32 v99, v100, v99
	v_sub_f32_e32 v100, v114, v99
	v_exp_f32_e32 v100, v100
	v_mov_b32_e32 v114, v99
	v_mul_f32_e32 v115, v115, v100
	v_pk_mul_f32 v[20:21], v[20:21], v[100:101] op_sel_hi:[1,0]
	v_pk_mul_f32 v[18:19], v[18:19], v[100:101] op_sel_hi:[1,0]
	v_pk_mul_f32 v[16:17], v[16:17], v[100:101] op_sel_hi:[1,0]
	v_pk_mul_f32 v[14:15], v[14:15], v[100:101] op_sel_hi:[1,0]
	v_pk_mul_f32 v[12:13], v[12:13], v[100:101] op_sel_hi:[1,0]
	v_pk_mul_f32 v[10:11], v[10:11], v[100:101] op_sel_hi:[1,0]
	v_pk_mul_f32 v[8:9], v[8:9], v[100:101] op_sel_hi:[1,0]
	v_pk_mul_f32 v[6:7], v[6:7], v[100:101] op_sel_hi:[1,0]
.LBB0_754:
	v_sub_f32_e32 v2, v90, v114
	v_sub_f32_e32 v4, v91, v114
	v_exp_f32_e32 v2, v2
	v_exp_f32_e32 v4, v4
	v_sub_f32_e32 v86, v86, v114
	v_sub_f32_e32 v5, v92, v114
	v_exp_f32_e32 v91, v86
	v_sub_f32_e32 v86, v87, v114
	v_exp_f32_e32 v5, v5
	v_sub_f32_e32 v90, v93, v114
	v_exp_f32_e32 v92, v86
	v_sub_f32_e32 v86, v88, v114
	v_exp_f32_e32 v90, v90
	v_exp_f32_e32 v93, v86
	v_sub_f32_e32 v86, v89, v114
	v_exp_f32_e32 v94, v86
	v_cvt_pk_bf16_f32 v86, v2, v4
	v_add_f32_e32 v2, v4, v2
	v_add_f32_e32 v2, v5, v2
	v_add_f32_e32 v2, v90, v2
	v_cvt_pk_bf16_f32 v87, v5, v90
	v_cvt_pk_bf16_f32 v88, v91, v92
	v_cvt_pk_bf16_f32 v89, v93, v94
	v_add_f32_e32 v2, v91, v2
	v_add_f32_e32 v2, v92, v2
	v_mfma_f32_16x16x32_bf16 v[18:21], v[82:85], v[86:89], v[18:21]
	v_add_f32_e32 v2, v93, v2
	v_add_f32_e32 v2, v94, v2
	v_add_f32_e32 v115, v115, v2
	v_mfma_f32_16x16x32_bf16 v[14:17], v[78:81], v[86:89], v[14:17]
	v_mfma_f32_16x16x32_bf16 v[10:13], v[74:77], v[86:89], v[10:13]
	v_mfma_f32_16x16x32_bf16 v[6:9], v[70:73], v[86:89], v[6:9]

.LBB0_758:
	s_min_i32 s6, s15, 5
	s_add_i32 s6, s6, s11
	s_waitcnt vmcnt(11)
	v_med3_i32 v54, s6, 0, 63
	v_lshl_or_b32 v2, v54, 11, v160
	v_lshl_add_u64 v[50:51], v[104:105], 0, v[2:3]
	v_lshlrev_b32_e32 v2, 12, v54
	s_waitcnt vmcnt(8)
	v_lshl_add_u64 v[66:67], v[106:107], 0, v[2:3]
	global_load_dwordx4 v[46:49], v[50:51], off
	s_nop 0
	global_load_dwordx4 v[50:53], v[50:51], off offset:1024
	s_nop 0
	global_load_dwordx4 v[54:57], v[66:67], off
	global_load_dwordx4 v[58:61], v[66:67], off offset:1024
	global_load_dwordx4 v[62:65], v[66:67], off offset:2048
	s_nop 0
	global_load_dwordx4 v[66:69], v[66:67], off offset:3072
	s_add_i32 s6, s10, s15
	s_add_i32 s6, s6, -3
	s_cmp_gt_u32 s6, 63
	s_cbranch_scc1 .LBB0_764
	ds_read2_b32 v[94:95], v5 offset1:1
	ds_read2_b32 v[96:97], v5 offset0:2 offset1:3
	ds_read2_b32 v[108:109], v5 offset0:16 offset1:17
	ds_read2_b32 v[110:111], v5 offset0:18 offset1:19
	s_waitcnt vmcnt(11) lgkmcnt(2)
	v_mfma_f32_16x16x32_fp8_fp8 v[94:97], v[90:91], v[38:39], v[94:97]
	v_mfma_f32_16x16x32_fp8_fp8 v[98:101], v[92:93], v[40:41], v[94:97]
	s_waitcnt vmcnt(10) lgkmcnt(0)
	v_mfma_f32_16x16x32_fp8_fp8 v[94:97], v[86:87], v[38:39], v[108:111]
	v_mfma_f32_16x16x32_fp8_fp8 v[94:97], v[88:89], v[40:41], v[94:97]
	s_nop 4
	v_max3_f32 v2, v98, v99, v100
	s_nop 1
	v_max3_f32 v109, v101, v94, v95
	v_max3_f32 v2, v2, v96, v97
	v_max_f32_e32 v2, v2, v109
	v_mov_b32_e32 v108, v2
	s_nop 1
	v_permlane16_swap_b32_e32 v2, v108
	v_max_f32_e32 v2, v2, v108
	v_mov_b32_e32 v108, v2
	s_nop 1
	v_permlane32_swap_b32_e32 v2, v108
	v_max_f32_e32 v2, v2, v108
	v_cmp_gt_f32_e32 vcc, v2, v112
	s_cbranch_vccz .LBB0_761
	v_max_f32_e32 v2, v2, v2
	v_max_f32_e32 v108, v112, v112
	v_max_f32_e32 v108, v108, v2
	v_sub_f32_e32 v2, v112, v108
	v_exp_f32_e32 v2, v2
	v_mov_b32_e32 v112, v108
	v_mul_f32_e32 v113, v113, v2
	v_pk_mul_f32 v[36:37], v[36:37], v[2:3] op_sel_hi:[1,0]
	v_pk_mul_f32 v[34:35], v[34:35], v[2:3] op_sel_hi:[1,0]
	v_pk_mul_f32 v[32:33], v[32:33], v[2:3] op_sel_hi:[1,0]
	v_pk_mul_f32 v[30:31], v[30:31], v[2:3] op_sel_hi:[1,0]
	v_pk_mul_f32 v[28:29], v[28:29], v[2:3] op_sel_hi:[1,0]
	v_pk_mul_f32 v[26:27], v[26:27], v[2:3] op_sel_hi:[1,0]
	v_pk_mul_f32 v[24:25], v[24:25], v[2:3] op_sel_hi:[1,0]
	v_pk_mul_f32 v[22:23], v[22:23], v[2:3] op_sel_hi:[1,0]
.LBB0_761:
	v_sub_f32_e32 v2, v98, v112
	v_sub_f32_e32 v98, v99, v112
	v_sub_f32_e32 v99, v100, v112
	v_sub_f32_e32 v100, v101, v112
	v_sub_f32_e32 v94, v94, v112
	v_sub_f32_e32 v95, v95, v112
	v_sub_f32_e32 v96, v96, v112
	v_sub_f32_e32 v97, v97, v112
	v_exp_f32_e32 v2, v2
	v_exp_f32_e32 v98, v98
	v_exp_f32_e32 v99, v99
	v_exp_f32_e32 v100, v100
	v_exp_f32_e32 v94, v94
	v_exp_f32_e32 v95, v95
	v_exp_f32_e32 v96, v96
	v_exp_f32_e32 v97, v97
	v_cvt_pk_bf16_f32 v108, v2, v98
	v_cvt_pk_bf16_f32 v109, v99, v100
	v_cvt_pk_bf16_f32 v110, v94, v95
	v_cvt_pk_bf16_f32 v111, v96, v97
	s_waitcnt vmcnt(9)
	s_nop 0
	v_mfma_f32_16x16x32_bf16 v[34:37], v[82:85], v[108:111], v[34:37]
	s_waitcnt vmcnt(8)
	v_mfma_f32_16x16x32_bf16 v[30:33], v[78:81], v[108:111], v[30:33]
	s_waitcnt vmcnt(7)
	v_mfma_f32_16x16x32_bf16 v[26:29], v[74:77], v[108:111], v[26:29]
	s_waitcnt vmcnt(6)
	v_mfma_f32_16x16x32_bf16 v[22:25], v[70:73], v[108:111], v[22:25]
	ds_read2_b32 v[108:109], v103 offset1:1
	ds_read2_b32 v[110:111], v103 offset0:2 offset1:3
	ds_read2_b32 v[116:117], v103 offset0:16 offset1:17
	ds_read2_b32 v[118:119], v103 offset0:18 offset1:19
	s_waitcnt lgkmcnt(2)
	v_mfma_f32_16x16x32_fp8_fp8 v[108:111], v[90:91], v[42:43], v[108:111]
	v_mfma_f32_16x16x32_fp8_fp8 v[90:93], v[92:93], v[44:45], v[108:111]
	s_waitcnt lgkmcnt(0)
	v_mfma_f32_16x16x32_fp8_fp8 v[108:111], v[86:87], v[42:43], v[116:119]
	v_mfma_f32_16x16x32_fp8_fp8 v[86:89], v[88:89], v[44:45], v[108:111]
	v_add_f32_e32 v2, v98, v2
	v_add_f32_e32 v2, v99, v2
	v_add_f32_e32 v2, v100, v2
	v_add_f32_e32 v2, v94, v2
	v_add_f32_e32 v2, v95, v2
	v_add_f32_e32 v2, v96, v2
	v_add_f32_e32 v2, v97, v2
	v_add_f32_e32 v113, v113, v2
	v_max3_f32 v101, v90, v91, v92
	v_max3_f32 v109, v93, v86, v87
	v_max3_f32 v101, v101, v88, v89
	v_max_f32_e32 v101, v101, v109
	v_mov_b32_e32 v108, v101
	s_nop 1
	v_permlane16_swap_b32_e32 v101, v108
	v_max_f32_e32 v101, v101, v108
	v_mov_b32_e32 v108, v101
	s_nop 1
	v_permlane32_swap_b32_e32 v101, v108
	v_max_f32_e32 v101, v101, v108
	v_cmp_gt_f32_e32 vcc, v101, v114
	s_cbranch_vccz .LBB0_763
	v_max_f32_e32 v101, v101, v101
	v_max_f32_e32 v108, v114, v114
	v_max_f32_e32 v101, v108, v101
	v_sub_f32_e32 v108, v114, v101
	v_exp_f32_e32 v108, v108
	v_mov_b32_e32 v114, v101
	v_mul_f32_e32 v115, v115, v108
	v_pk_mul_f32 v[20:21], v[20:21], v[108:109] op_sel_hi:[1,0]
	v_pk_mul_f32 v[18:19], v[18:19], v[108:109] op_sel_hi:[1,0]
	v_pk_mul_f32 v[16:17], v[16:17], v[108:109] op_sel_hi:[1,0]
	v_pk_mul_f32 v[14:15], v[14:15], v[108:109] op_sel_hi:[1,0]
	v_pk_mul_f32 v[12:13], v[12:13], v[108:109] op_sel_hi:[1,0]
	v_pk_mul_f32 v[10:11], v[10:11], v[108:109] op_sel_hi:[1,0]
	v_pk_mul_f32 v[8:9], v[8:9], v[108:109] op_sel_hi:[1,0]
	v_pk_mul_f32 v[6:7], v[6:7], v[108:109] op_sel_hi:[1,0]
.LBB0_763:
	v_sub_f32_e32 v2, v90, v114
	v_sub_f32_e32 v90, v91, v114
	v_exp_f32_e32 v2, v2
	v_exp_f32_e32 v90, v90
	v_sub_f32_e32 v86, v86, v114
	v_sub_f32_e32 v91, v92, v114
	v_sub_f32_e32 v92, v93, v114
	v_exp_f32_e32 v93, v86
	v_sub_f32_e32 v86, v87, v114
	v_exp_f32_e32 v91, v91
	v_exp_f32_e32 v94, v86
	v_sub_f32_e32 v86, v88, v114
	v_exp_f32_e32 v92, v92
	v_exp_f32_e32 v95, v86
	v_sub_f32_e32 v86, v89, v114
	v_exp_f32_e32 v96, v86
	v_cvt_pk_bf16_f32 v86, v2, v90
	v_add_f32_e32 v2, v90, v2
	v_add_f32_e32 v2, v91, v2
	v_add_f32_e32 v2, v92, v2
	v_cvt_pk_bf16_f32 v87, v91, v92
	v_cvt_pk_bf16_f32 v88, v93, v94
	v_cvt_pk_bf16_f32 v89, v95, v96
	v_add_f32_e32 v2, v93, v2
	v_add_f32_e32 v2, v94, v2
	v_mfma_f32_16x16x32_bf16 v[18:21], v[82:85], v[86:89], v[18:21]
	v_add_f32_e32 v2, v95, v2
	v_add_f32_e32 v2, v96, v2
	v_add_f32_e32 v115, v115, v2
	v_mfma_f32_16x16x32_bf16 v[14:17], v[78:81], v[86:89], v[14:17]
	v_mfma_f32_16x16x32_bf16 v[10:13], v[74:77], v[86:89], v[10:13]
	v_mfma_f32_16x16x32_bf16 v[6:9], v[70:73], v[86:89], v[6:9]

.LBB0_784:
	s_or_b32 s15, s69, 8
	v_or_b32_e32 v5, s15, v118
	v_mul_u32_u24_e32 v46, 0xf00, v5
	v_mov_b32_e32 v47, v3
	v_lshl_add_u64 v[46:47], s[92:93], 0, v[46:47]
	s_lshl_b32 s92, s15, 15
	s_add_u32 s10, s10, s92
	s_addc_u32 s11, s11, 0
	v_lshl_add_u64 v[112:113], s[10:11], 0, v[154:155]
	s_lshl_b32 s10, s15, 16
	s_add_u32 s10, s30, s10
	s_addc_u32 s11, s31, 0
	v_mov_b32_e32 v5, v3
	v_lshl_add_u64 v[4:5], s[10:11], 0, v[4:5]
	v_mov_b32_e32 v103, v3
	v_lshl_add_u64 v[46:47], v[46:47], 0, v[154:155]
	v_lshl_add_u64 v[4:5], v[4:5], 0, v[102:103]
	v_lshl_add_u64 v[46:47], v[46:47], 0, s[64:65]
	s_waitcnt vmcnt(6)
	v_lshl_add_u64 v[50:51], v[112:113], 0, v[110:111]
	v_lshl_add_u64 v[52:53], v[4:5], 0, s[60:61]
	global_load_dwordx4 v[46:49], v[46:47], off offset:2048 nt
	s_nop 0
	global_load_dwordx4 v[66:69], v[50:51], off
	global_load_dwordx4 v[74:77], v[50:51], off offset:1024
	global_load_dwordx4 v[62:65], v[52:53], off
	global_load_dwordx4 v[58:61], v[52:53], off offset:1024
	global_load_dwordx4 v[54:57], v[52:53], off offset:2048
	s_nop 0
	global_load_dwordx4 v[50:53], v[52:53], off offset:3072
	s_andn2_b64 vcc, exec, s[62:63]
	s_cbranch_vccnz .LBB0_788
	v_mov_b32_e32 v105, v3
	s_waitcnt vmcnt(8)
	v_lshl_add_u64 v[70:71], v[4:5], 0, s[96:97]
	v_lshl_add_u64 v[90:91], v[112:113], 0, v[104:105]
	global_load_dwordx4 v[86:89], v[70:71], off
	global_load_dwordx4 v[82:85], v[70:71], off offset:1024
	global_load_dwordx4 v[78:81], v[70:71], off offset:2048
	s_nop 0
	global_load_dwordx4 v[70:73], v[70:71], off offset:3072
	s_nop 0
	global_load_dwordx4 v[94:97], v[90:91], off offset:1024
	s_nop 0
	global_load_dwordx4 v[90:93], v[90:91], off
	s_add_i32 s10, s76, s78
	v_lshl_add_u32 v98, v116, 2, s10
	v_add_u32_e32 v99, 0xa560, v98
	v_add_u32_e32 v100, 0xa568, v98
	v_add_u32_e32 v102, 0xa5a0, v98
	v_add_u32_e32 v104, 0xa5a8, v98
	ds_read2_b32 v[98:99], v99 offset1:1
	ds_read2_b32 v[100:101], v100 offset1:1
	ds_read2_b32 v[102:103], v102 offset1:1
	ds_read2_b32 v[104:105], v104 offset1:1
	s_waitcnt vmcnt(0) lgkmcnt(2)
	v_mfma_f32_16x16x32_fp8_fp8 v[98:101], v[90:91], v[46:47], v[98:101]
	v_mfma_f32_16x16x32_fp8_fp8 v[90:93], v[92:93], v[48:49], v[98:101]
	s_waitcnt lgkmcnt(0)
	v_mfma_f32_16x16x32_fp8_fp8 v[98:101], v[94:95], v[46:47], v[102:105]
	v_mfma_f32_16x16x32_fp8_fp8 v[94:97], v[96:97], v[48:49], v[98:101]
	s_nop 6
	v_max_f32_e32 v98, v91, v91
	v_max_f32_e32 v99, v90, v90
	v_max_f32_e32 v98, v99, v98
	v_max_f32_e32 v99, v93, v93
	v_max_f32_e32 v100, v92, v92
	v_max_f32_e32 v99, v100, v99
	v_max_f32_e32 v100, v97, v97
	v_max_f32_e32 v101, v96, v96
	v_max_f32_e32 v100, v101, v100
	v_max3_f32 v100, v94, v95, v100
	v_max3_f32 v98, v98, v99, v100
	v_mov_b32_e32 v99, v98
	s_nop 1
	v_permlane16_swap_b32_e32 v98, v99
	v_max_f32_e32 v98, v98, v99
	v_mov_b32_e32 v99, v98
	s_nop 1
	v_permlane32_swap_b32_e32 v98, v99
	v_max_f32_e32 v98, v98, v99
	v_cmp_gt_f32_e32 vcc, v98, v114
	s_cbranch_vccz .LBB0_787
	v_max_f32_e32 v98, v98, v98
	v_max_f32_e32 v99, v114, v114
	v_max_f32_e32 v99, v99, v98
	v_sub_f32_e32 v98, v114, v99
	v_exp_f32_e32 v98, v98
	v_mov_b32_e32 v114, v99
	v_mul_f32_e32 v115, v115, v98
	v_pk_mul_f32 v[20:21], v[20:21], v[98:99] op_sel_hi:[1,0]
	v_pk_mul_f32 v[18:19], v[18:19], v[98:99] op_sel_hi:[1,0]
	v_pk_mul_f32 v[16:17], v[16:17], v[98:99] op_sel_hi:[1,0]
	v_pk_mul_f32 v[14:15], v[14:15], v[98:99] op_sel_hi:[1,0]
	v_pk_mul_f32 v[12:13], v[12:13], v[98:99] op_sel_hi:[1,0]
	v_pk_mul_f32 v[10:11], v[10:11], v[98:99] op_sel_hi:[1,0]
	v_pk_mul_f32 v[8:9], v[8:9], v[98:99] op_sel_hi:[1,0]
	v_pk_mul_f32 v[6:7], v[6:7], v[98:99] op_sel_hi:[1,0]

.LBB0_806:
	s_min_u32 s8, s7, 8
	s_add_i32 s8, s8, s6
	v_med3_i32 v5, s8, 0, v184
	v_lshl_or_b32 v2, v5, 11, v160
	v_lshl_add_u64 v[94:95], v[172:173], 0, v[2:3]
	v_lshlrev_b32_e32 v2, 12, v5
	v_lshl_add_u64 v[122:123], v[174:175], 0, v[2:3]
	global_load_dwordx4 v[90:93], v[94:95], off
	s_nop 0
	global_load_dwordx4 v[94:97], v[94:95], off offset:1024
	s_nop 0
	global_load_dwordx4 v[106:109], v[122:123], off
	global_load_dwordx4 v[110:113], v[122:123], off offset:1024
	global_load_dwordx4 v[118:121], v[122:123], off offset:2048
	s_nop 0
	global_load_dwordx4 v[122:125], v[122:123], off offset:3072
	s_add_i32 s8, s6, s7
	s_add_i32 s8, s8, -1
	s_cmpk_gt_u32 s8, 0xff
	s_cbranch_scc1 .LBB0_816
	ds_read2_b32 v[134:135], v190 offset1:1
	ds_read2_b32 v[136:137], v190 offset0:2 offset1:3
	ds_read2_b32 v[192:193], v190 offset0:16 offset1:17
	ds_read2_b32 v[194:195], v190 offset0:18 offset1:19
	s_waitcnt vmcnt(11) lgkmcnt(2)
	v_mfma_f32_16x16x32_fp8_fp8 v[134:137], v[130:131], v[70:71], v[134:137]
	v_mfma_f32_16x16x32_fp8_fp8 v[138:141], v[132:133], v[72:73], v[134:137]
	s_waitcnt vmcnt(10) lgkmcnt(0)
	v_mfma_f32_16x16x32_fp8_fp8 v[134:137], v[126:127], v[70:71], v[192:195]
	v_mfma_f32_16x16x32_fp8_fp8 v[134:137], v[128:129], v[72:73], v[134:137]
	s_nop 4
	v_max3_f32 v2, v138, v139, v140
	s_nop 1
	v_max3_f32 v191, v141, v134, v135
	v_max3_f32 v2, v2, v136, v137
	v_max_f32_e32 v2, v2, v191
	v_mov_b32_e32 v5, v2
	s_nop 1
	v_permlane16_swap_b32_e32 v2, v5
	v_max_f32_e32 v2, v2, v5
	v_mov_b32_e32 v5, v2
	s_nop 1
	v_permlane32_swap_b32_e32 v2, v5
	v_max_f32_e32 v2, v2, v5
	v_cmp_gt_f32_e32 vcc, v2, v176
	s_cbranch_vccz .LBB0_809
	v_max_f32_e32 v2, v2, v2
	v_max_f32_e32 v5, v176, v176
	v_max_f32_e32 v5, v5, v2
	v_sub_f32_e32 v2, v176, v5
	v_exp_f32_e32 v2, v2
	v_mov_b32_e32 v176, v5
	v_mul_f32_e32 v4, v4, v2
	v_pk_mul_f32 v[68:69], v[68:69], v[2:3] op_sel_hi:[1,0]
	v_pk_mul_f32 v[66:67], v[66:67], v[2:3] op_sel_hi:[1,0]
	v_pk_mul_f32 v[64:65], v[64:65], v[2:3] op_sel_hi:[1,0]
	v_pk_mul_f32 v[62:63], v[62:63], v[2:3] op_sel_hi:[1,0]
	v_pk_mul_f32 v[60:61], v[60:61], v[2:3] op_sel_hi:[1,0]
	v_pk_mul_f32 v[58:59], v[58:59], v[2:3] op_sel_hi:[1,0]
	v_pk_mul_f32 v[56:57], v[56:57], v[2:3] op_sel_hi:[1,0]
	v_pk_mul_f32 v[54:55], v[54:55], v[2:3] op_sel_hi:[1,0]
.LBB0_809:
	v_sub_f32_e32 v134, v134, v176
	v_exp_f32_e32 v193, v134
	v_sub_f32_e32 v134, v135, v176
	v_sub_f32_e32 v2, v138, v176
	v_sub_f32_e32 v138, v140, v176
	v_exp_f32_e32 v194, v134
	v_sub_f32_e32 v134, v136, v176
	v_sub_f32_e32 v5, v139, v176
	v_exp_f32_e32 v191, v138
	v_sub_f32_e32 v138, v141, v176
	v_exp_f32_e32 v195, v134
	v_sub_f32_e32 v134, v137, v176
	v_exp_f32_e32 v2, v2
	v_exp_f32_e32 v5, v5
	v_exp_f32_e32 v192, v138
	v_exp_f32_e32 v196, v134
	v_cvt_pk_bf16_f32 v136, v193, v194
	v_cvt_pk_bf16_f32 v134, v2, v5
	v_cvt_pk_bf16_f32 v135, v191, v192
	v_cvt_pk_bf16_f32 v137, v195, v196
	s_waitcnt vmcnt(9)
	s_nop 0
	v_mfma_f32_16x16x32_bf16 v[66:69], v[114:117], v[134:137], v[66:69]
	s_waitcnt vmcnt(8)
	v_mfma_f32_16x16x32_bf16 v[62:65], v[102:105], v[134:137], v[62:65]
	s_waitcnt vmcnt(7)
	v_mfma_f32_16x16x32_bf16 v[58:61], v[98:101], v[134:137], v[58:61]
	s_waitcnt vmcnt(6)
	v_mfma_f32_16x16x32_bf16 v[54:57], v[86:89], v[134:137], v[54:57]
	v_add_u32_e32 v134, 0x504, v190
	v_add_u32_e32 v136, 0x50c, v190
	ds_read2_b32 v[134:135], v134 offset1:1
	ds_read2_b32 v[136:137], v136 offset1:1
	v_add_u32_e32 v138, 0x544, v190
	ds_read2_b32 v[198:199], v138 offset1:1
	v_add_u32_e32 v138, 0x54c, v190
	ds_read2_b32 v[200:201], v138 offset1:1
	s_waitcnt lgkmcnt(2)
	v_mfma_f32_16x16x32_fp8_fp8 v[134:137], v[130:131], v[74:75], v[134:137]
	v_mfma_f32_16x16x32_fp8_fp8 v[138:141], v[132:133], v[76:77], v[134:137]
	s_waitcnt lgkmcnt(0)
	v_mfma_f32_16x16x32_fp8_fp8 v[134:137], v[126:127], v[74:75], v[198:201]
	v_mfma_f32_16x16x32_fp8_fp8 v[134:137], v[128:129], v[76:77], v[134:137]
	s_nop 4
	v_max3_f32 v197, v138, v139, v140
	s_nop 1
	v_max3_f32 v199, v141, v134, v135
	v_max3_f32 v197, v197, v136, v137
	v_max_f32_e32 v197, v197, v199
	v_mov_b32_e32 v198, v197
	s_nop 1
	v_permlane16_swap_b32_e32 v197, v198
	v_max_f32_e32 v197, v197, v198
	v_mov_b32_e32 v198, v197
	s_nop 1
	v_permlane32_swap_b32_e32 v197, v198
	v_max_f32_e32 v197, v197, v198
	v_cmp_gt_f32_e32 vcc, v197, v177
	s_cbranch_vccz .LBB0_811
	v_max_f32_e32 v197, v197, v197
	v_max_f32_e32 v198, v177, v177
	v_max_f32_e32 v197, v198, v197
	v_sub_f32_e32 v177, v177, v197
	v_exp_f32_e32 v198, v177
	v_mov_b32_e32 v177, v197
	v_mul_f32_e32 v189, v189, v198
	v_pk_mul_f32 v[52:53], v[52:53], v[198:199] op_sel_hi:[1,0]
	v_pk_mul_f32 v[50:51], v[50:51], v[198:199] op_sel_hi:[1,0]
	v_pk_mul_f32 v[48:49], v[48:49], v[198:199] op_sel_hi:[1,0]
	v_pk_mul_f32 v[46:47], v[46:47], v[198:199] op_sel_hi:[1,0]
	v_pk_mul_f32 v[44:45], v[44:45], v[198:199] op_sel_hi:[1,0]
	v_pk_mul_f32 v[42:43], v[42:43], v[198:199] op_sel_hi:[1,0]
	v_pk_mul_f32 v[40:41], v[40:41], v[198:199] op_sel_hi:[1,0]
	v_pk_mul_f32 v[38:39], v[38:39], v[198:199] op_sel_hi:[1,0]
.LBB0_811:
	v_sub_f32_e32 v138, v138, v177
	v_sub_f32_e32 v134, v134, v177
	v_exp_f32_e32 v197, v138
	v_sub_f32_e32 v138, v139, v177
	v_exp_f32_e32 v201, v134
	v_sub_f32_e32 v134, v135, v177
	v_exp_f32_e32 v198, v138
	v_sub_f32_e32 v138, v140, v177
	v_exp_f32_e32 v202, v134
	v_sub_f32_e32 v134, v136, v177
	v_exp_f32_e32 v199, v138
	v_sub_f32_e32 v138, v141, v177
	v_exp_f32_e32 v203, v134
	v_sub_f32_e32 v134, v137, v177
	v_exp_f32_e32 v200, v138
	v_exp_f32_e32 v204, v134
	v_cvt_pk_bf16_f32 v134, v197, v198
	v_cvt_pk_bf16_f32 v136, v201, v202
	v_cvt_pk_bf16_f32 v135, v199, v200
	v_cvt_pk_bf16_f32 v137, v203, v204
	s_nop 1
	v_mfma_f32_16x16x32_bf16 v[50:53], v[114:117], v[134:137], v[50:53]
	v_mfma_f32_16x16x32_bf16 v[46:49], v[102:105], v[134:137], v[46:49]
	v_mfma_f32_16x16x32_bf16 v[42:45], v[98:101], v[134:137], v[42:45]
	v_mfma_f32_16x16x32_bf16 v[38:41], v[86:89], v[134:137], v[38:41]
	v_add_u32_e32 v134, 0xa08, v190
	v_add_u32_e32 v136, 0xa10, v190
	ds_read2_b32 v[134:135], v134 offset1:1
	ds_read2_b32 v[136:137], v136 offset1:1
	v_add_u32_e32 v138, 0xa48, v190
	ds_read2_b32 v[206:207], v138 offset1:1
	v_add_u32_e32 v138, 0xa50, v190
	ds_read2_b32 v[208:209], v138 offset1:1
	s_waitcnt lgkmcnt(2)
	v_mfma_f32_16x16x32_fp8_fp8 v[134:137], v[130:131], v[78:79], v[134:137]
	v_mfma_f32_16x16x32_fp8_fp8 v[138:141], v[132:133], v[80:81], v[134:137]
	s_waitcnt lgkmcnt(0)
	v_mfma_f32_16x16x32_fp8_fp8 v[134:137], v[126:127], v[78:79], v[206:209]
	v_mfma_f32_16x16x32_fp8_fp8 v[134:137], v[128:129], v[80:81], v[134:137]
	s_nop 4
	v_max3_f32 v205, v138, v139, v140
	s_nop 1
	v_max3_f32 v207, v141, v134, v135
	v_max3_f32 v205, v205, v136, v137
	v_max_f32_e32 v205, v205, v207
	v_mov_b32_e32 v206, v205
	s_nop 1
	v_permlane16_swap_b32_e32 v205, v206
	v_max_f32_e32 v205, v205, v206
	v_mov_b32_e32 v206, v205
	s_nop 1
	v_permlane32_swap_b32_e32 v205, v206
	v_max_f32_e32 v205, v205, v206
	v_cmp_gt_f32_e32 vcc, v205, v178
	s_cbranch_vccz .LBB0_813
	v_max_f32_e32 v205, v205, v205
	v_max_f32_e32 v206, v178, v178
	v_max_f32_e32 v205, v206, v205
	v_sub_f32_e32 v178, v178, v205
	v_exp_f32_e32 v178, v178
	s_nop 0
	v_mul_f32_e32 v188, v188, v178
	v_pk_mul_f32 v[36:37], v[36:37], v[178:179] op_sel_hi:[1,0]
	v_pk_mul_f32 v[34:35], v[34:35], v[178:179] op_sel_hi:[1,0]
	v_pk_mul_f32 v[32:33], v[32:33], v[178:179] op_sel_hi:[1,0]
	v_pk_mul_f32 v[30:31], v[30:31], v[178:179] op_sel_hi:[1,0]
	v_pk_mul_f32 v[28:29], v[28:29], v[178:179] op_sel_hi:[1,0]
	v_pk_mul_f32 v[26:27], v[26:27], v[178:179] op_sel_hi:[1,0]
	v_pk_mul_f32 v[24:25], v[24:25], v[178:179] op_sel_hi:[1,0]
	v_pk_mul_f32 v[22:23], v[22:23], v[178:179] op_sel_hi:[1,0]
	v_mov_b32_e32 v178, v205

.LBB0_815:
	v_add_f32_e32 v138, v139, v138
	v_add_f32_e32 v138, v140, v138
	v_add_f32_e32 v138, v141, v138
	v_add_f32_e32 v134, v134, v138
	v_add_f32_e32 v134, v135, v134
	v_add_f32_e32 v2, v5, v2
	v_add_f32_e32 v134, v136, v134
	v_add_f32_e32 v2, v191, v2
	v_add_f32_e32 v134, v137, v134
	v_add_f32_e32 v2, v192, v2
	v_add_f32_e32 v188, v188, v134
	v_add_f32_e32 v134, 0, v197
	v_add_f32_e32 v2, v193, v2
	v_add_f32_e32 v134, v198, v134
	v_add_f32_e32 v2, v194, v2
	v_add_f32_e32 v134, v199, v134
	v_add_f32_e32 v2, v195, v2
	v_add_f32_e32 v134, v200, v134
	v_add_f32_e32 v2, v196, v2
	v_add_f32_e32 v134, v201, v134
	v_add_f32_e32 v4, v4, v2
	v_sub_f32_e32 v2, v130, v179
	v_sub_f32_e32 v5, v131, v179
	v_add_f32_e32 v134, v202, v134
	v_exp_f32_e32 v2, v2
	v_exp_f32_e32 v5, v5
	v_sub_f32_e32 v126, v126, v179
	v_add_f32_e32 v134, v203, v134
	v_sub_f32_e32 v130, v132, v179
	v_exp_f32_e32 v132, v126
	v_sub_f32_e32 v126, v127, v179
	v_add_f32_e32 v134, v204, v134
	v_exp_f32_e32 v130, v130
	v_sub_f32_e32 v131, v133, v179
	v_exp_f32_e32 v133, v126
	v_sub_f32_e32 v126, v128, v179
	v_add_f32_e32 v189, v189, v134
	v_exp_f32_e32 v131, v131
	v_exp_f32_e32 v134, v126
	v_sub_f32_e32 v126, v129, v179
	v_exp_f32_e32 v135, v126
	v_cvt_pk_bf16_f32 v126, v2, v5
	v_add_f32_e32 v2, v5, v2
	v_add_f32_e32 v2, v130, v2
	v_add_f32_e32 v2, v131, v2
	v_cvt_pk_bf16_f32 v127, v130, v131
	v_cvt_pk_bf16_f32 v128, v132, v133
	v_cvt_pk_bf16_f32 v129, v134, v135
	v_add_f32_e32 v2, v132, v2
	v_add_f32_e32 v2, v133, v2
	v_mfma_f32_16x16x32_bf16 v[18:21], v[114:117], v[126:129], v[18:21]
	v_add_f32_e32 v2, v134, v2
	v_add_f32_e32 v2, v135, v2
	v_add_f32_e32 v187, v187, v2
	v_mfma_f32_16x16x32_bf16 v[14:17], v[102:105], v[126:129], v[14:17]
	v_mfma_f32_16x16x32_bf16 v[10:13], v[98:101], v[126:129], v[10:13]
	v_mfma_f32_16x16x32_bf16 v[6:9], v[86:89], v[126:129], v[6:9]
